# speedup vs baseline: 1.0019x; 1.0019x over previous
.LBB1_25:
	s_add_i32 s51, s45, s24
	s_add_i32 s51, s51, 2
	s_sub_i32 s51, s51, s50
	s_cmp_ge_i32 s51, 1
	s_cbranch_scc1 .Lfqk_0a
	v_add_u32_e32 v186, s22, v209
	ds_read_b64_tr_b16 v[182:183], v186 offset:24576
	ds_read_b64_tr_b16 v[184:185], v186 offset:25088
	s_waitcnt lgkmcnt(9)
	v_mfma_f32_32x32x16_f16 v[98:113], v[174:177], v[142:145], v[34:49]
	v_add_f32_e32 v82, v66, v67
	v_add_f32_e32 v82, v68, v82
	v_add_f32_e32 v82, v69, v82
	v_add_f32_e32 v82, v70, v82
	v_add_f32_e32 v82, v71, v82
	v_cvt_pk_f16_f32 v134, v66, v67
	v_cvt_pk_f16_f32 v135, v68, v69
	ds_read_b64_tr_b16 v[174:175], v186 offset:28672
	ds_read_b64_tr_b16 v[176:177], v186 offset:29184
	v_add_f32_e32 v66, v72, v82
	s_waitcnt lgkmcnt(10)
	v_mfma_f32_32x32x16_f16 v[82:97], v[170:173], v[142:145], v[34:49]
	v_add_f32_e32 v66, v73, v66
	v_add_f32_e32 v66, v74, v66
	v_add_f32_e32 v66, v75, v66
	v_cvt_pk_f16_f32 v136, v70, v71
	v_cvt_pk_f16_f32 v137, v72, v73
	ds_read_b64_tr_b16 v[178:179], v186 offset:25600
	ds_read_b64_tr_b16 v[180:181], v186 offset:26112
	s_waitcnt lgkmcnt(11)
	v_mfma_f32_32x32x16_f16 v[98:113], v[166:169], v[138:141], v[98:113]
	v_add_f32_e32 v66, v76, v66
	v_add_f32_e32 v66, v77, v66
	v_add_f32_e32 v66, v78, v66
	v_add_f32_e32 v66, v79, v66
	v_cvt_pk_f16_f32 v126, v74, v75
	v_cvt_pk_f16_f32 v127, v76, v77
	ds_read_b64_tr_b16 v[74:75], v186 offset:29696
	ds_read_b64_tr_b16 v[76:77], v186 offset:30208
	s_waitcnt lgkmcnt(12)
	v_mfma_f32_32x32x16_f16 v[82:97], v[162:165], v[138:141], v[82:97]
	v_add_f32_e32 v66, v80, v66
	v_add_f32_e32 v66, v81, v66
	v_add_f32_e32 v66, v50, v66
	v_add_f32_e32 v66, v51, v66
	v_cvt_pk_f16_f32 v128, v78, v79
	v_cvt_pk_f16_f32 v129, v80, v81
	ds_read_b64_tr_b16 v[70:71], v186 offset:26624
	ds_read_b64_tr_b16 v[72:73], v186 offset:27136
	s_waitcnt lgkmcnt(13)
	v_mfma_f32_32x32x16_f16 v[98:113], v[158:161], v[130:133], v[98:113]
	v_add_f32_e32 v66, v52, v66
	v_add_f32_e32 v66, v53, v66
	v_add_f32_e32 v66, v54, v66
	v_add_f32_e32 v78, v55, v66
	v_cvt_pk_f16_f32 v118, v50, v51
	v_cvt_pk_f16_f32 v119, v52, v53
	ds_read_b64_tr_b16 v[66:67], v186 offset:30720
	ds_read_b64_tr_b16 v[68:69], v186 offset:31232
	s_waitcnt lgkmcnt(14)
	v_mfma_f32_32x32x16_f16 v[82:97], v[154:157], v[130:133], v[82:97]
	v_add_f32_e32 v50, v56, v78
	v_add_f32_e32 v50, v57, v50
	v_add_f32_e32 v50, v58, v50
	v_add_f32_e32 v50, v59, v50
	v_cvt_pk_f16_f32 v120, v54, v55
	v_cvt_pk_f16_f32 v121, v56, v57
	ds_read_b64_tr_b16 v[54:55], v186 offset:27648
	ds_read_b64_tr_b16 v[56:57], v186 offset:28160
	s_waitcnt lgkmcnt(14)
	v_mfma_f32_32x32x16_f16 v[98:113], v[150:153], v[122:125], v[98:113]
	v_add_f32_e32 v50, v60, v50
	v_add_f32_e32 v50, v61, v50
	v_add_f32_e32 v50, v62, v50
	v_add_f32_e32 v78, v63, v50
	v_cvt_pk_f16_f32 v114, v58, v59
	v_cvt_pk_f16_f32 v115, v60, v61
	ds_read_b64_tr_b16 v[50:51], v186 offset:31744
	ds_read_b64_tr_b16 v[52:53], v186 offset:32256
	v_mfma_f32_32x32x16_f16 v[82:97], v[146:149], v[122:125], v[82:97]
	v_add_f32_e32 v58, v64, v78
	v_add_f32_e32 v58, v65, v58
	v_add_f32_e32 v58, 0, v58
	v_cvt_pk_f16_f32 v116, v62, v63
	v_cvt_pk_f16_f32 v117, v64, v65
.Lsqk_0a:
	s_add_i32 s2, s24, 1
	s_cmp_ge_u32 s2, s41
	s_cselect_b64 s[20:21], -1, 0
	s_and_b64 vcc, exec, s[20:21]
	s_cbranch_vccnz .LBB1_27
	s_add_u32 s2, s16, 0xffffe000
	s_addc_u32 s3, s17, -1
	s_add_i32 s22, s43, s39
	s_mov_b32 s23, m0
	s_mov_b32 m0, s22
	s_nop 0
	global_load_lds_dwordx4 v211, s[2:3]
	s_mov_b32 m0, s23

.LBB1_74:
	s_cmp_lt_u32 s50, 2
	s_cbranch_scc1 .Lfin0_skip
	s_cmp_eq_u32 s50, 2
	s_cbranch_scc1 .Lmfill_0f
	v_add_u32_e32 v100, s44, v209
	ds_read_b64_tr_b16 v[178:179], v100 offset:24576
	ds_read_b64_tr_b16 v[180:181], v100 offset:25088
	v_add_f32_e32 v82, v66, v67
	v_add_f32_e32 v82, v68, v82
	v_add_f32_e32 v82, v69, v82
	v_add_f32_e32 v82, v70, v82
	v_add_f32_e32 v98, v71, v82
	s_waitcnt lgkmcnt(9)
	v_mfma_f32_32x32x16_f16 v[82:97], v[174:177], v[142:145], v[34:49]
	v_cvt_pk_f16_f32 v134, v66, v67
	v_cvt_pk_f16_f32 v135, v68, v69
	ds_read_b64_tr_b16 v[174:175], v100 offset:28672
	ds_read_b64_tr_b16 v[176:177], v100 offset:29184
	s_waitcnt lgkmcnt(10)
	v_mfma_f32_32x32x16_f16 v[34:49], v[170:173], v[142:145], v[34:49]
	v_add_f32_e32 v66, v72, v98
	v_add_f32_e32 v66, v73, v66
	v_add_f32_e32 v66, v74, v66
	v_add_f32_e32 v66, v75, v66
	v_cvt_pk_f16_f32 v136, v70, v71
	v_cvt_pk_f16_f32 v137, v72, v73
	ds_read_b64_tr_b16 v[170:171], v100 offset:25600
	ds_read_b64_tr_b16 v[172:173], v100 offset:26112
	s_waitcnt lgkmcnt(11)
	v_mfma_f32_32x32x16_f16 v[82:97], v[166:169], v[138:141], v[82:97]
	v_add_f32_e32 v66, v76, v66
	v_add_f32_e32 v66, v77, v66
	v_add_f32_e32 v66, v78, v66
	v_add_f32_e32 v66, v79, v66
	v_cvt_pk_f16_f32 v126, v74, v75
	v_cvt_pk_f16_f32 v127, v76, v77
	ds_read_b64_tr_b16 v[142:143], v100 offset:29696
	ds_read_b64_tr_b16 v[144:145], v100 offset:30208
	s_waitcnt lgkmcnt(12)
	v_mfma_f32_32x32x16_f16 v[34:49], v[162:165], v[138:141], v[34:49]
	v_add_f32_e32 v66, v80, v66
	v_add_f32_e32 v66, v81, v66
	v_add_f32_e32 v66, v50, v66
	v_add_f32_e32 v66, v51, v66
	v_cvt_pk_f16_f32 v128, v78, v79
	v_cvt_pk_f16_f32 v129, v80, v81
	ds_read_b64_tr_b16 v[110:111], v100 offset:26624
	ds_read_b64_tr_b16 v[112:113], v100 offset:27136
	s_waitcnt lgkmcnt(13)
	v_mfma_f32_32x32x16_f16 v[82:97], v[158:161], v[130:133], v[82:97]
	v_add_f32_e32 v66, v52, v66
	v_add_f32_e32 v66, v53, v66
	v_add_f32_e32 v66, v54, v66
	v_add_f32_e32 v66, v55, v66
	v_cvt_pk_f16_f32 v118, v50, v51
	v_cvt_pk_f16_f32 v119, v52, v53
	ds_read_b64_tr_b16 v[106:107], v100 offset:30720
	ds_read_b64_tr_b16 v[108:109], v100 offset:31232
	s_waitcnt lgkmcnt(14)
	v_mfma_f32_32x32x16_f16 v[34:49], v[154:157], v[130:133], v[34:49]
	v_add_f32_e32 v50, v56, v66
	v_add_f32_e32 v50, v57, v50
	v_add_f32_e32 v50, v58, v50
	v_add_f32_e32 v50, v59, v50
	v_cvt_pk_f16_f32 v120, v54, v55
	v_cvt_pk_f16_f32 v121, v56, v57
	ds_read_b64_tr_b16 v[102:103], v100 offset:27648
	ds_read_b64_tr_b16 v[104:105], v100 offset:28160
	s_waitcnt lgkmcnt(14)
	v_mfma_f32_32x32x16_f16 v[82:97], v[150:153], v[122:125], v[82:97]
	v_add_f32_e32 v50, v60, v50
	v_add_f32_e32 v50, v61, v50
	v_add_f32_e32 v50, v62, v50
	v_add_f32_e32 v50, v63, v50
	v_cvt_pk_f16_f32 v114, v58, v59
	v_cvt_pk_f16_f32 v115, v60, v61
	ds_read_b64_tr_b16 v[98:99], v100 offset:31744
	ds_read_b64_tr_b16 v[100:101], v100 offset:32256
	v_mfma_f32_32x32x16_f16 v[34:49], v[146:149], v[122:125], v[34:49]
	v_add_f32_e32 v50, v64, v50
	v_add_f32_e32 v50, v65, v50
	v_add_f32_e32 v66, 0, v50
	v_cvt_pk_f16_f32 v116, v62, v63
	v_cvt_pk_f16_f32 v117, v64, v65
	v_or_b32_e32 v214, 0xe0, v210
	v_or_b32_e32 v213, 0xc0, v210
	v_mov_b32_e32 v67, 0xff800000
	v_cmp_le_u32_e32 vcc, v214, v204
	v_or_b32_e32 v215, 0xe1, v210
	v_or_b32_e32 v216, 0xc2, v210
	s_nop 0
	v_cndmask_b32_e32 v34, v67, v34, vcc
	v_cmp_lt_u32_e32 vcc, v213, v204
	v_or_b32_e32 v217, 0xe2, v210
	v_or_b32_e32 v218, 0xc3, v210
	v_cndmask_b32_e32 v51, v67, v83, vcc
	v_cmp_le_u32_e32 vcc, v213, v204
	v_or_b32_e32 v219, 0xe3, v210
	v_or_b32_e32 v220, 0xc8, v210
	v_cndmask_b32_e32 v50, v67, v82, vcc
	v_cmp_le_u32_e32 vcc, v215, v204
	v_or_b32_e32 v221, 0xe8, v210
	v_or_b32_e32 v222, 0xc9, v210
	v_cndmask_b32_e32 v35, v67, v35, vcc
	v_cmp_le_u32_e32 vcc, v216, v204
	v_or_b32_e32 v223, 0xe9, v210
	v_or_b32_e32 v224, 0xca, v210
	v_cndmask_b32_e32 v52, v67, v84, vcc
	v_cmp_le_u32_e32 vcc, v217, v204
	v_or_b32_e32 v225, 0xea, v210
	v_or_b32_e32 v226, 0xcb, v210
	v_cndmask_b32_e32 v36, v67, v36, vcc
	v_cmp_le_u32_e32 vcc, v218, v204
	v_or_b32_e32 v227, 0xeb, v210
	v_or_b32_e32 v228, 0xd0, v210
	v_cndmask_b32_e32 v53, v67, v85, vcc
	v_cmp_le_u32_e32 vcc, v219, v204
	v_or_b32_e32 v229, 0xf0, v210
	v_or_b32_e32 v230, 0xd1, v210
	v_cndmask_b32_e32 v37, v67, v37, vcc
	v_cmp_le_u32_e32 vcc, v220, v204
	v_or_b32_e32 v231, 0xf1, v210
	v_or_b32_e32 v232, 0xd2, v210
	v_cndmask_b32_e32 v54, v67, v86, vcc
	v_cmp_le_u32_e32 vcc, v221, v204
	v_or_b32_e32 v233, 0xf2, v210
	v_or_b32_e32 v234, 0xd3, v210
	v_cndmask_b32_e32 v38, v67, v38, vcc
	v_cmp_le_u32_e32 vcc, v222, v204
	v_or_b32_e32 v235, 0xf3, v210
	v_or_b32_e32 v236, 0xd8, v210
	v_cndmask_b32_e32 v55, v67, v87, vcc
	v_cmp_le_u32_e32 vcc, v223, v204
	v_or_b32_e32 v237, 0xf8, v210
	v_or_b32_e32 v238, 0xd9, v210
	v_cndmask_b32_e32 v39, v67, v39, vcc
	v_cmp_le_u32_e32 vcc, v224, v204
	v_or_b32_e32 v239, 0xf9, v210
	v_or_b32_e32 v240, 0xda, v210
	v_cndmask_b32_e32 v56, v67, v88, vcc
	v_cmp_le_u32_e32 vcc, v225, v204
	v_or_b32_e32 v241, 0xfa, v210
	v_or_b32_e32 v242, 0xdb, v210
	v_cndmask_b32_e32 v40, v67, v40, vcc
	v_cmp_le_u32_e32 vcc, v226, v204
	v_or_b32_e32 v243, 0xfb, v210
	v_max_f32_e32 v68, v50, v50
	v_cndmask_b32_e32 v57, v67, v89, vcc
	v_cmp_le_u32_e32 vcc, v227, v204
	v_add_f32_e32 v82, v203, v66
	s_mov_b32 s2, 0x41000000
	v_cndmask_b32_e32 v41, v67, v41, vcc
	v_cmp_le_u32_e32 vcc, v228, v204
	s_nop 1
	v_cndmask_b32_e32 v58, v67, v90, vcc
	v_cmp_le_u32_e32 vcc, v229, v204
	s_nop 1
	v_cndmask_b32_e32 v42, v67, v42, vcc
	v_cmp_le_u32_e32 vcc, v230, v204
	s_nop 1
	v_cndmask_b32_e32 v59, v67, v91, vcc
	v_cmp_le_u32_e32 vcc, v231, v204
	s_nop 1
	v_cndmask_b32_e32 v43, v67, v43, vcc
	v_cmp_le_u32_e32 vcc, v232, v204
	s_nop 1
	v_cndmask_b32_e32 v60, v67, v92, vcc
	v_cmp_le_u32_e32 vcc, v233, v204
	s_nop 1
	v_cndmask_b32_e32 v44, v67, v44, vcc
	v_cmp_le_u32_e32 vcc, v234, v204
	s_nop 1
	v_cndmask_b32_e32 v61, v67, v93, vcc
	v_cmp_le_u32_e32 vcc, v235, v204
	s_nop 1
	v_cndmask_b32_e32 v45, v67, v45, vcc
	v_cmp_le_u32_e32 vcc, v236, v204
	s_nop 1
	v_cndmask_b32_e32 v62, v67, v94, vcc
	v_cmp_le_u32_e32 vcc, v237, v204
	s_nop 1
	v_cndmask_b32_e32 v46, v67, v46, vcc
	v_cmp_le_u32_e32 vcc, v238, v204
	s_nop 1
	v_cndmask_b32_e32 v63, v67, v95, vcc
	v_cmp_le_u32_e32 vcc, v239, v204
	s_nop 1
	v_cndmask_b32_e32 v47, v67, v47, vcc
	v_cmp_le_u32_e32 vcc, v240, v204
	s_nop 1
	v_cndmask_b32_e32 v64, v67, v96, vcc
	v_cmp_le_u32_e32 vcc, v241, v204
	s_nop 1
	v_cndmask_b32_e32 v48, v67, v48, vcc
	v_cmp_le_u32_e32 vcc, v242, v204
	s_nop 1
	v_cndmask_b32_e32 v65, v67, v97, vcc
	v_cmp_le_u32_e32 vcc, v243, v204
	s_nop 1
	v_cndmask_b32_e32 v49, v67, v49, vcc

.LBB1_103:
	s_cmp_lt_u32 s50, 2
	s_cbranch_scc1 .Lfin1_skip
	s_cmp_eq_u32 s50, 2
	s_cbranch_scc1 .Lmfill_1f
	v_add_u32_e32 v65, s26, v251
	ds_read_b64_tr_b16 v[124:125], v65
	ds_read_b64_tr_b16 v[126:127], v65 offset:512
	s_waitcnt lgkmcnt(9)
	v_mfma_f32_32x32x16_f16 v[96:111], v[188:191], v[140:143], v[32:47]
	v_add_f32_e32 v66, v80, v81
	v_add_f32_e32 v66, v82, v66
	v_add_f32_e32 v66, v83, v66
	v_add_f32_e32 v66, v84, v66
	v_add_f32_e32 v66, v85, v66
	v_cvt_pk_f16_f32 v156, v80, v81
	v_cvt_pk_f16_f32 v157, v82, v83
	ds_read_b64_tr_b16 v[120:121], v65 offset:4096
	ds_read_b64_tr_b16 v[122:123], v65 offset:4608
	s_waitcnt lgkmcnt(10)
	v_mfma_f32_32x32x16_f16 v[32:47], v[184:187], v[140:143], v[32:47]
	v_add_f32_e32 v66, v86, v66
	v_add_f32_e32 v66, v87, v66
	v_add_f32_e32 v66, v88, v66
	v_add_f32_e32 v66, v89, v66
	v_cvt_pk_f16_f32 v158, v84, v85
	v_cvt_pk_f16_f32 v159, v86, v87
	ds_read_b64_tr_b16 v[116:117], v65 offset:1024
	ds_read_b64_tr_b16 v[118:119], v65 offset:1536
	s_waitcnt lgkmcnt(11)
	v_mfma_f32_32x32x16_f16 v[96:111], v[180:183], v[136:139], v[96:111]
	v_add_f32_e32 v66, v90, v66
	v_add_f32_e32 v66, v91, v66
	v_add_f32_e32 v66, v92, v66
	v_add_f32_e32 v66, v93, v66
	v_cvt_pk_f16_f32 v152, v88, v89
	v_cvt_pk_f16_f32 v153, v90, v91
	ds_read_b64_tr_b16 v[112:113], v65 offset:5120
	ds_read_b64_tr_b16 v[114:115], v65 offset:5632
	s_waitcnt lgkmcnt(12)
	v_mfma_f32_32x32x16_f16 v[32:47], v[176:179], v[136:139], v[32:47]
	v_add_f32_e32 v66, v94, v66
	v_add_f32_e32 v66, v95, v66
	v_add_f32_e32 v66, v48, v66
	v_add_f32_e32 v66, v49, v66
	v_cvt_pk_f16_f32 v154, v92, v93
	v_cvt_pk_f16_f32 v155, v94, v95
	ds_read_b64_tr_b16 v[92:93], v65 offset:2048
	ds_read_b64_tr_b16 v[94:95], v65 offset:2560
	s_waitcnt lgkmcnt(13)
	v_mfma_f32_32x32x16_f16 v[96:111], v[172:175], v[132:135], v[96:111]
	v_add_f32_e32 v66, v50, v66
	v_add_f32_e32 v66, v51, v66
	v_add_f32_e32 v66, v52, v66
	v_add_f32_e32 v66, v53, v66
	v_cvt_pk_f16_f32 v148, v48, v49
	v_cvt_pk_f16_f32 v149, v50, v51
	ds_read_b64_tr_b16 v[88:89], v65 offset:6144
	ds_read_b64_tr_b16 v[90:91], v65 offset:6656
	s_waitcnt lgkmcnt(14)
	v_mfma_f32_32x32x16_f16 v[32:47], v[168:171], v[132:135], v[32:47]
	v_add_f32_e32 v48, v54, v66
	v_add_f32_e32 v48, v55, v48
	v_add_f32_e32 v48, v56, v48
	v_add_f32_e32 v48, v57, v48
	v_cvt_pk_f16_f32 v150, v52, v53
	v_cvt_pk_f16_f32 v151, v54, v55
	ds_read_b64_tr_b16 v[84:85], v65 offset:3072
	ds_read_b64_tr_b16 v[86:87], v65 offset:3584
	s_waitcnt lgkmcnt(14)
	v_mfma_f32_32x32x16_f16 v[96:111], v[164:167], v[128:131], v[96:111]
	v_add_f32_e32 v48, v58, v48
	v_add_f32_e32 v48, v59, v48
	v_add_f32_e32 v48, v60, v48
	v_add_f32_e32 v48, v61, v48
	v_cvt_pk_f16_f32 v144, v56, v57
	v_cvt_pk_f16_f32 v145, v58, v59
	ds_read_b64_tr_b16 v[80:81], v65 offset:7168
	ds_read_b64_tr_b16 v[82:83], v65 offset:7680
	v_mfma_f32_32x32x16_f16 v[32:47], v[160:163], v[128:131], v[32:47]
	v_add_f32_e32 v48, v62, v48
	v_add_f32_e32 v48, v63, v48
	v_add_f32_e32 v65, 0, v48
	v_cvt_pk_f16_f32 v146, v60, v61
	v_cvt_pk_f16_f32 v147, v62, v63
	v_mov_b32_e32 v66, 0xff800000
	v_cmp_le_u32_e32 vcc, v214, v207
	s_mov_b32 s2, 0x41000000
	s_nop 3
	v_cndmask_b32_e32 v32, v66, v32, vcc
	v_cmp_lt_u32_e32 vcc, v213, v207
	s_nop 1
	v_cndmask_b32_e32 v49, v66, v97, vcc
	v_cmp_le_u32_e32 vcc, v213, v207
	s_nop 1
	v_cndmask_b32_e32 v48, v66, v96, vcc
	v_cmp_le_u32_e32 vcc, v215, v207
	v_max_f32_e32 v67, v48, v48
	v_add_f32_e32 v96, v64, v65
	v_cndmask_b32_e32 v33, v66, v33, vcc
	v_cmp_le_u32_e32 vcc, v216, v207
	s_nop 1
	v_cndmask_b32_e32 v50, v66, v98, vcc
	v_cmp_le_u32_e32 vcc, v217, v207
	s_nop 1
	v_cndmask_b32_e32 v34, v66, v34, vcc
	v_cmp_le_u32_e32 vcc, v218, v207
	s_nop 1
	v_cndmask_b32_e32 v51, v66, v99, vcc
	v_cmp_le_u32_e32 vcc, v219, v207
	s_nop 1
	v_cndmask_b32_e32 v35, v66, v35, vcc
	v_cmp_le_u32_e32 vcc, v220, v207
	s_nop 1
	v_cndmask_b32_e32 v52, v66, v100, vcc
	v_cmp_le_u32_e32 vcc, v221, v207
	s_nop 1
	v_cndmask_b32_e32 v36, v66, v36, vcc
	v_cmp_le_u32_e32 vcc, v222, v207
	s_nop 1
	v_cndmask_b32_e32 v53, v66, v101, vcc
	v_cmp_le_u32_e32 vcc, v223, v207
	s_nop 1
	v_cndmask_b32_e32 v37, v66, v37, vcc
	v_cmp_le_u32_e32 vcc, v224, v207
	s_nop 1
	v_cndmask_b32_e32 v54, v66, v102, vcc
	v_cmp_le_u32_e32 vcc, v225, v207
	s_nop 1
	v_cndmask_b32_e32 v38, v66, v38, vcc
	v_cmp_le_u32_e32 vcc, v226, v207
	s_nop 1
	v_cndmask_b32_e32 v55, v66, v103, vcc
	v_cmp_le_u32_e32 vcc, v227, v207
	s_nop 1
	v_cndmask_b32_e32 v39, v66, v39, vcc
	v_cmp_le_u32_e32 vcc, v228, v207
	s_nop 1
	v_cndmask_b32_e32 v56, v66, v104, vcc
	v_cmp_le_u32_e32 vcc, v229, v207
	s_nop 1
	v_cndmask_b32_e32 v40, v66, v40, vcc
	v_cmp_le_u32_e32 vcc, v230, v207
	s_nop 1
	v_cndmask_b32_e32 v57, v66, v105, vcc
	v_cmp_le_u32_e32 vcc, v231, v207
	s_nop 1
	v_cndmask_b32_e32 v41, v66, v41, vcc
	v_cmp_le_u32_e32 vcc, v232, v207
	s_nop 1
	v_cndmask_b32_e32 v58, v66, v106, vcc
	v_cmp_le_u32_e32 vcc, v233, v207
	s_nop 1
	v_cndmask_b32_e32 v42, v66, v42, vcc
	v_cmp_le_u32_e32 vcc, v234, v207
	s_nop 1
	v_cndmask_b32_e32 v59, v66, v107, vcc
	v_cmp_le_u32_e32 vcc, v235, v207
	s_nop 1
	v_cndmask_b32_e32 v43, v66, v43, vcc
	v_cmp_le_u32_e32 vcc, v236, v207
	s_nop 1
	v_cndmask_b32_e32 v60, v66, v108, vcc
	v_cmp_le_u32_e32 vcc, v237, v207
	s_nop 1
	v_cndmask_b32_e32 v44, v66, v44, vcc
	v_cmp_le_u32_e32 vcc, v238, v207
	s_nop 1
	v_cndmask_b32_e32 v61, v66, v109, vcc
	v_cmp_le_u32_e32 vcc, v239, v207
	s_nop 1
	v_cndmask_b32_e32 v45, v66, v45, vcc
	v_cmp_le_u32_e32 vcc, v240, v207
	s_nop 1
	v_cndmask_b32_e32 v62, v66, v110, vcc
	v_cmp_le_u32_e32 vcc, v241, v207
	s_nop 1
	v_cndmask_b32_e32 v46, v66, v46, vcc
	v_cmp_le_u32_e32 vcc, v242, v207
	s_nop 1
	v_cndmask_b32_e32 v63, v66, v111, vcc
	v_cmp_le_u32_e32 vcc, v243, v207
	s_nop 1
	v_cndmask_b32_e32 v47, v66, v47, vcc

.LBB1_112:
	s_add_i32 s51, s27, s31
	s_add_i32 s51, s51, 2
	s_sub_i32 s51, s51, s50
	s_cmp_ge_i32 s51, 1
	s_cbranch_scc1 .Lfqk_1a
	v_add_u32_e32 v196, s12, v251
	ds_read_b64_tr_b16 v[192:193], v196
	ds_read_b64_tr_b16 v[194:195], v196 offset:512
	s_waitcnt lgkmcnt(9)
	v_mfma_f32_32x32x16_f16 v[112:127], v[188:191], v[140:143], v[32:47]
	v_add_f32_e32 v66, v80, v81
	v_add_f32_e32 v66, v82, v66
	v_add_f32_e32 v66, v83, v66
	v_add_f32_e32 v66, v84, v66
	v_add_f32_e32 v66, v85, v66
	v_cvt_pk_f16_f32 v156, v80, v81
	v_cvt_pk_f16_f32 v157, v82, v83
	ds_read_b64_tr_b16 v[188:189], v196 offset:4096
	ds_read_b64_tr_b16 v[190:191], v196 offset:4608
	s_waitcnt lgkmcnt(10)
	v_mfma_f32_32x32x16_f16 v[96:111], v[184:187], v[140:143], v[32:47]
	v_add_f32_e32 v66, v86, v66
	v_add_f32_e32 v66, v87, v66
	v_add_f32_e32 v66, v88, v66
	v_add_f32_e32 v66, v89, v66
	v_cvt_pk_f16_f32 v158, v84, v85
	v_cvt_pk_f16_f32 v159, v86, v87
	ds_read_b64_tr_b16 v[78:79], v196 offset:1024
	ds_read_b64_tr_b16 v[80:81], v196 offset:1536
	s_waitcnt lgkmcnt(11)
	v_mfma_f32_32x32x16_f16 v[112:127], v[180:183], v[136:139], v[112:127]
	v_add_f32_e32 v66, v90, v66
	v_add_f32_e32 v66, v91, v66
	v_add_f32_e32 v66, v92, v66
	v_add_f32_e32 v66, v93, v66
	v_cvt_pk_f16_f32 v152, v88, v89
	v_cvt_pk_f16_f32 v153, v90, v91
	ds_read_b64_tr_b16 v[74:75], v196 offset:5120
	ds_read_b64_tr_b16 v[76:77], v196 offset:5632
	s_waitcnt lgkmcnt(12)
	v_mfma_f32_32x32x16_f16 v[96:111], v[176:179], v[136:139], v[96:111]
	v_add_f32_e32 v66, v94, v66
	v_add_f32_e32 v66, v95, v66
	v_add_f32_e32 v66, v48, v66
	v_add_f32_e32 v66, v49, v66
	v_cvt_pk_f16_f32 v154, v92, v93
	v_cvt_pk_f16_f32 v155, v94, v95
	ds_read_b64_tr_b16 v[70:71], v196 offset:2048
	ds_read_b64_tr_b16 v[72:73], v196 offset:2560
	s_waitcnt lgkmcnt(13)
	v_mfma_f32_32x32x16_f16 v[112:127], v[172:175], v[132:135], v[112:127]
	v_add_f32_e32 v66, v50, v66
	v_add_f32_e32 v66, v51, v66
	v_add_f32_e32 v66, v52, v66
	v_add_f32_e32 v82, v53, v66
	v_cvt_pk_f16_f32 v148, v48, v49
	v_cvt_pk_f16_f32 v149, v50, v51
	ds_read_b64_tr_b16 v[66:67], v196 offset:6144
	ds_read_b64_tr_b16 v[68:69], v196 offset:6656
	s_waitcnt lgkmcnt(14)
	v_mfma_f32_32x32x16_f16 v[96:111], v[168:171], v[132:135], v[96:111]
	v_add_f32_e32 v48, v54, v82
	v_add_f32_e32 v48, v55, v48
	v_add_f32_e32 v48, v56, v48
	v_add_f32_e32 v48, v57, v48
	v_cvt_pk_f16_f32 v150, v52, v53
	v_cvt_pk_f16_f32 v151, v54, v55
	ds_read_b64_tr_b16 v[52:53], v196 offset:3072
	ds_read_b64_tr_b16 v[54:55], v196 offset:3584
	s_waitcnt lgkmcnt(14)
	v_mfma_f32_32x32x16_f16 v[112:127], v[164:167], v[128:131], v[112:127]
	v_add_f32_e32 v48, v58, v48
	v_add_f32_e32 v48, v59, v48
	v_add_f32_e32 v48, v60, v48
	v_add_f32_e32 v82, v61, v48
	v_cvt_pk_f16_f32 v144, v56, v57
	v_cvt_pk_f16_f32 v145, v58, v59
	ds_read_b64_tr_b16 v[48:49], v196 offset:7168
	ds_read_b64_tr_b16 v[50:51], v196 offset:7680
	v_mfma_f32_32x32x16_f16 v[96:111], v[160:163], v[128:131], v[96:111]
	v_add_f32_e32 v56, v62, v82
	v_add_f32_e32 v56, v63, v56
	v_add_f32_e32 v56, 0, v56
	v_cvt_pk_f16_f32 v146, v60, v61
	v_cvt_pk_f16_f32 v147, v62, v63
.Lsqk_1a:
	s_add_i32 s2, s31, 1
	s_cmp_ge_u32 s2, s24
	s_cselect_b64 s[8:9], -1, 0
	s_and_b64 vcc, exec, s[8:9]
	s_cbranch_vccnz .LBB1_114
	s_add_u32 s2, s6, 0xffffe000
	s_addc_u32 s3, s7, -1
	s_add_i32 s12, s25, s22
	s_mov_b32 s13, m0
	s_mov_b32 m0, s12
	s_nop 0
	global_load_lds_dwordx4 v211, s[2:3]
	s_mov_b32 m0, s13

.Lmfill_0f:
	v_add_u32_e32 v100, s44, v209
	ds_read_b64_tr_b16 v[178:179], v100 offset:24576
	ds_read_b64_tr_b16 v[180:181], v100 offset:25088
	v_add_f32_e32 v82, v66, v67
	v_add_f32_e32 v82, v68, v82
	v_add_f32_e32 v82, v69, v82
	v_add_f32_e32 v82, v70, v82
	v_add_f32_e32 v98, v71, v82
	v_cvt_pk_f16_f32 v134, v66, v67
	v_cvt_pk_f16_f32 v135, v68, v69
	ds_read_b64_tr_b16 v[174:175], v100 offset:28672
	ds_read_b64_tr_b16 v[176:177], v100 offset:29184
	v_add_f32_e32 v66, v72, v98
	v_add_f32_e32 v66, v73, v66
	v_add_f32_e32 v66, v74, v66
	v_add_f32_e32 v66, v75, v66
	v_cvt_pk_f16_f32 v136, v70, v71
	v_cvt_pk_f16_f32 v137, v72, v73
	ds_read_b64_tr_b16 v[170:171], v100 offset:25600
	ds_read_b64_tr_b16 v[172:173], v100 offset:26112
	v_add_f32_e32 v66, v76, v66
	v_add_f32_e32 v66, v77, v66
	v_add_f32_e32 v66, v78, v66
	v_add_f32_e32 v66, v79, v66
	v_cvt_pk_f16_f32 v126, v74, v75
	v_cvt_pk_f16_f32 v127, v76, v77
	ds_read_b64_tr_b16 v[142:143], v100 offset:29696
	ds_read_b64_tr_b16 v[144:145], v100 offset:30208
	v_add_f32_e32 v66, v80, v66
	v_add_f32_e32 v66, v81, v66
	v_add_f32_e32 v66, v50, v66
	v_add_f32_e32 v66, v51, v66
	v_cvt_pk_f16_f32 v128, v78, v79
	v_cvt_pk_f16_f32 v129, v80, v81
	ds_read_b64_tr_b16 v[110:111], v100 offset:26624
	ds_read_b64_tr_b16 v[112:113], v100 offset:27136
	v_add_f32_e32 v66, v52, v66
	v_add_f32_e32 v66, v53, v66
	v_add_f32_e32 v66, v54, v66
	v_add_f32_e32 v66, v55, v66
	v_cvt_pk_f16_f32 v118, v50, v51
	v_cvt_pk_f16_f32 v119, v52, v53
	ds_read_b64_tr_b16 v[106:107], v100 offset:30720
	ds_read_b64_tr_b16 v[108:109], v100 offset:31232
	v_add_f32_e32 v50, v56, v66
	v_add_f32_e32 v50, v57, v50
	v_add_f32_e32 v50, v58, v50
	v_add_f32_e32 v50, v59, v50
	v_cvt_pk_f16_f32 v120, v54, v55
	v_cvt_pk_f16_f32 v121, v56, v57
	ds_read_b64_tr_b16 v[102:103], v100 offset:27648
	ds_read_b64_tr_b16 v[104:105], v100 offset:28160
	v_add_f32_e32 v50, v60, v50
	v_add_f32_e32 v50, v61, v50
	v_add_f32_e32 v50, v62, v50
	v_add_f32_e32 v50, v63, v50
	v_cvt_pk_f16_f32 v114, v58, v59
	v_cvt_pk_f16_f32 v115, v60, v61
	ds_read_b64_tr_b16 v[98:99], v100 offset:31744
	ds_read_b64_tr_b16 v[100:101], v100 offset:32256
	v_add_f32_e32 v50, v64, v50
	v_add_f32_e32 v50, v65, v50
	v_add_f32_e32 v66, 0, v50
	v_cvt_pk_f16_f32 v116, v62, v63
	v_cvt_pk_f16_f32 v117, v64, v65
	v_mov_b32_e32 v34, 0
	v_mov_b32_e32 v35, 0
	v_mov_b32_e32 v36, 0
	v_mov_b32_e32 v37, 0
	v_mov_b32_e32 v38, 0
	v_mov_b32_e32 v39, 0
	v_mov_b32_e32 v40, 0
	v_mov_b32_e32 v41, 0
	v_mov_b32_e32 v42, 0
	v_mov_b32_e32 v43, 0
	v_mov_b32_e32 v44, 0
	v_mov_b32_e32 v45, 0
	v_mov_b32_e32 v46, 0
	v_mov_b32_e32 v47, 0
	v_mov_b32_e32 v48, 0
	v_mov_b32_e32 v49, 0
	v_mov_b32_e32 v50, 0
	v_mov_b32_e32 v51, 0
	v_mov_b32_e32 v52, 0
	v_mov_b32_e32 v53, 0
	v_mov_b32_e32 v54, 0
	v_mov_b32_e32 v55, 0
	v_mov_b32_e32 v56, 0
	v_mov_b32_e32 v57, 0
	v_mov_b32_e32 v58, 0
	v_mov_b32_e32 v59, 0
	v_mov_b32_e32 v60, 0
	v_mov_b32_e32 v61, 0
	v_mov_b32_e32 v62, 0
	v_mov_b32_e32 v63, 0
	v_mov_b32_e32 v64, 0
	v_mov_b32_e32 v65, 0
	v_add_f32_e32 v82, v203, v66
	v_lshl_add_u32 v66, v210, 2, s38
	s_waitcnt lgkmcnt(0)
	v_mfma_f32_32x32x16_f16 v[2:17], v[134:137], v[178:181], v[2:17]
	v_mfma_f32_32x32x16_f16 v[18:33], v[134:137], v[174:177], v[18:33]
	v_mfma_f32_32x32x16_f16 v[2:17], v[126:129], v[170:173], v[2:17]
	v_mfma_f32_32x32x16_f16 v[18:33], v[126:129], v[142:145], v[18:33]
	v_mfma_f32_32x32x16_f16 v[2:17], v[118:121], v[110:113], v[2:17]
	v_mfma_f32_32x32x16_f16 v[18:33], v[118:121], v[106:109], v[18:33]
	v_mfma_f32_32x32x16_f16 v[2:17], v[114:117], v[102:105], v[2:17]
	v_mfma_f32_32x32x16_f16 v[18:33], v[114:117], v[98:101], v[18:33]
	s_mov_b32 s3, 0
	s_cmp_lt_i32 s36, 0
	s_branch .Lfin0_land
.Lmfill_1f:
	v_add_u32_e32 v65, s26, v251
	ds_read_b64_tr_b16 v[124:125], v65
	ds_read_b64_tr_b16 v[126:127], v65 offset:512
	v_add_f32_e32 v66, v80, v81
	v_add_f32_e32 v66, v82, v66
	v_add_f32_e32 v66, v83, v66
	v_add_f32_e32 v66, v84, v66
	v_add_f32_e32 v66, v85, v66
	v_cvt_pk_f16_f32 v156, v80, v81
	v_cvt_pk_f16_f32 v157, v82, v83
	ds_read_b64_tr_b16 v[120:121], v65 offset:4096
	ds_read_b64_tr_b16 v[122:123], v65 offset:4608
	v_add_f32_e32 v66, v86, v66
	v_add_f32_e32 v66, v87, v66
	v_add_f32_e32 v66, v88, v66
	v_add_f32_e32 v66, v89, v66
	v_cvt_pk_f16_f32 v158, v84, v85
	v_cvt_pk_f16_f32 v159, v86, v87
	ds_read_b64_tr_b16 v[116:117], v65 offset:1024
	ds_read_b64_tr_b16 v[118:119], v65 offset:1536
	v_add_f32_e32 v66, v90, v66
	v_add_f32_e32 v66, v91, v66
	v_add_f32_e32 v66, v92, v66
	v_add_f32_e32 v66, v93, v66
	v_cvt_pk_f16_f32 v152, v88, v89
	v_cvt_pk_f16_f32 v153, v90, v91
	ds_read_b64_tr_b16 v[112:113], v65 offset:5120
	ds_read_b64_tr_b16 v[114:115], v65 offset:5632
	v_add_f32_e32 v66, v94, v66
	v_add_f32_e32 v66, v95, v66
	v_add_f32_e32 v66, v48, v66
	v_add_f32_e32 v66, v49, v66
	v_cvt_pk_f16_f32 v154, v92, v93
	v_cvt_pk_f16_f32 v155, v94, v95
	ds_read_b64_tr_b16 v[92:93], v65 offset:2048
	ds_read_b64_tr_b16 v[94:95], v65 offset:2560
	v_add_f32_e32 v66, v50, v66
	v_add_f32_e32 v66, v51, v66
	v_add_f32_e32 v66, v52, v66
	v_add_f32_e32 v66, v53, v66
	v_cvt_pk_f16_f32 v148, v48, v49
	v_cvt_pk_f16_f32 v149, v50, v51
	ds_read_b64_tr_b16 v[88:89], v65 offset:6144
	ds_read_b64_tr_b16 v[90:91], v65 offset:6656
	v_add_f32_e32 v48, v54, v66
	v_add_f32_e32 v48, v55, v48
	v_add_f32_e32 v48, v56, v48
	v_add_f32_e32 v48, v57, v48
	v_cvt_pk_f16_f32 v150, v52, v53
	v_cvt_pk_f16_f32 v151, v54, v55
	ds_read_b64_tr_b16 v[84:85], v65 offset:3072
	ds_read_b64_tr_b16 v[86:87], v65 offset:3584
	v_add_f32_e32 v48, v58, v48
	v_add_f32_e32 v48, v59, v48
	v_add_f32_e32 v48, v60, v48
	v_add_f32_e32 v48, v61, v48
	v_cvt_pk_f16_f32 v144, v56, v57
	v_cvt_pk_f16_f32 v145, v58, v59
	ds_read_b64_tr_b16 v[80:81], v65 offset:7168
	ds_read_b64_tr_b16 v[82:83], v65 offset:7680
	v_add_f32_e32 v48, v62, v48
	v_add_f32_e32 v48, v63, v48
	v_add_f32_e32 v65, 0, v48
	v_cvt_pk_f16_f32 v146, v60, v61
	v_cvt_pk_f16_f32 v147, v62, v63
	v_add_f32_e32 v65, v64, v65
	v_lshl_add_u32 v64, v210, 2, s21
	s_waitcnt lgkmcnt(0)
	v_mfma_f32_32x32x16_f16 v[0:15], v[156:159], v[124:127], v[0:15]
	v_mfma_f32_32x32x16_f16 v[16:31], v[156:159], v[120:123], v[16:31]
	v_mfma_f32_32x32x16_f16 v[0:15], v[152:155], v[116:119], v[0:15]
	v_mfma_f32_32x32x16_f16 v[16:31], v[152:155], v[112:115], v[16:31]
	v_mfma_f32_32x32x16_f16 v[0:15], v[148:151], v[92:95], v[0:15]
	v_mfma_f32_32x32x16_f16 v[16:31], v[148:151], v[88:91], v[16:31]
	v_mfma_f32_32x32x16_f16 v[0:15], v[144:147], v[84:87], v[0:15]
	v_mfma_f32_32x32x16_f16 v[16:31], v[144:147], v[80:83], v[16:31]
	v_mov_b32_e32 v32, v65
	s_nop 1
	v_permlane32_swap_b32_e32 v65, v32
	s_branch .Lfin1_land
.Lfqk_1a:
	v_add_u32_e32 v196, s12, v251
	ds_read_b64_tr_b16 v[192:193], v196
	ds_read_b64_tr_b16 v[194:195], v196 offset:512
	v_add_f32_e32 v66, v80, v81
	v_add_f32_e32 v66, v82, v66
	v_add_f32_e32 v66, v83, v66
	v_add_f32_e32 v66, v84, v66
	v_add_f32_e32 v66, v85, v66
	v_cvt_pk_f16_f32 v156, v80, v81
	v_cvt_pk_f16_f32 v157, v82, v83
	ds_read_b64_tr_b16 v[188:189], v196 offset:4096
	ds_read_b64_tr_b16 v[190:191], v196 offset:4608
	v_add_f32_e32 v66, v86, v66
	v_add_f32_e32 v66, v87, v66
	v_add_f32_e32 v66, v88, v66
	v_add_f32_e32 v66, v89, v66
	v_cvt_pk_f16_f32 v158, v84, v85
	v_cvt_pk_f16_f32 v159, v86, v87
	ds_read_b64_tr_b16 v[78:79], v196 offset:1024
	ds_read_b64_tr_b16 v[80:81], v196 offset:1536
	v_add_f32_e32 v66, v90, v66
	v_add_f32_e32 v66, v91, v66
	v_add_f32_e32 v66, v92, v66
	v_add_f32_e32 v66, v93, v66
	v_cvt_pk_f16_f32 v152, v88, v89
	v_cvt_pk_f16_f32 v153, v90, v91
	ds_read_b64_tr_b16 v[74:75], v196 offset:5120
	ds_read_b64_tr_b16 v[76:77], v196 offset:5632
	v_add_f32_e32 v66, v94, v66
	v_add_f32_e32 v66, v95, v66
	v_add_f32_e32 v66, v48, v66
	v_add_f32_e32 v66, v49, v66
	v_cvt_pk_f16_f32 v154, v92, v93
	v_cvt_pk_f16_f32 v155, v94, v95
	ds_read_b64_tr_b16 v[70:71], v196 offset:2048
	ds_read_b64_tr_b16 v[72:73], v196 offset:2560
	v_add_f32_e32 v66, v50, v66
	v_add_f32_e32 v66, v51, v66
	v_add_f32_e32 v66, v52, v66
	v_add_f32_e32 v82, v53, v66
	v_cvt_pk_f16_f32 v148, v48, v49
	v_cvt_pk_f16_f32 v149, v50, v51
	ds_read_b64_tr_b16 v[66:67], v196 offset:6144
	ds_read_b64_tr_b16 v[68:69], v196 offset:6656
	v_add_f32_e32 v48, v54, v82
	v_add_f32_e32 v48, v55, v48
	v_add_f32_e32 v48, v56, v48
	v_add_f32_e32 v48, v57, v48
	v_cvt_pk_f16_f32 v150, v52, v53
	v_cvt_pk_f16_f32 v151, v54, v55
	ds_read_b64_tr_b16 v[52:53], v196 offset:3072
	ds_read_b64_tr_b16 v[54:55], v196 offset:3584
	v_add_f32_e32 v48, v58, v48
	v_add_f32_e32 v48, v59, v48
	v_add_f32_e32 v48, v60, v48
	v_add_f32_e32 v82, v61, v48
	v_cvt_pk_f16_f32 v144, v56, v57
	v_cvt_pk_f16_f32 v145, v58, v59
	ds_read_b64_tr_b16 v[48:49], v196 offset:7168
	ds_read_b64_tr_b16 v[50:51], v196 offset:7680
	v_add_f32_e32 v56, v62, v82
	v_add_f32_e32 v56, v63, v56
	v_add_f32_e32 v56, 0, v56
	v_cvt_pk_f16_f32 v146, v60, v61
	v_cvt_pk_f16_f32 v147, v62, v63
	s_branch .Lsqk_1a
.Lfqk_0a:
	v_add_u32_e32 v186, s22, v209
	ds_read_b64_tr_b16 v[182:183], v186 offset:24576
	ds_read_b64_tr_b16 v[184:185], v186 offset:25088
	v_add_f32_e32 v82, v66, v67
	v_add_f32_e32 v82, v68, v82
	v_add_f32_e32 v82, v69, v82
	v_add_f32_e32 v82, v70, v82
	v_add_f32_e32 v82, v71, v82
	v_cvt_pk_f16_f32 v134, v66, v67
	v_cvt_pk_f16_f32 v135, v68, v69
	ds_read_b64_tr_b16 v[174:175], v186 offset:28672
	ds_read_b64_tr_b16 v[176:177], v186 offset:29184
	v_add_f32_e32 v66, v72, v82
	v_add_f32_e32 v66, v73, v66
	v_add_f32_e32 v66, v74, v66
	v_add_f32_e32 v66, v75, v66
	v_cvt_pk_f16_f32 v136, v70, v71
	v_cvt_pk_f16_f32 v137, v72, v73
	ds_read_b64_tr_b16 v[178:179], v186 offset:25600
	ds_read_b64_tr_b16 v[180:181], v186 offset:26112
	v_add_f32_e32 v66, v76, v66
	v_add_f32_e32 v66, v77, v66
	v_add_f32_e32 v66, v78, v66
	v_add_f32_e32 v66, v79, v66
	v_cvt_pk_f16_f32 v126, v74, v75
	v_cvt_pk_f16_f32 v127, v76, v77
	ds_read_b64_tr_b16 v[74:75], v186 offset:29696
	ds_read_b64_tr_b16 v[76:77], v186 offset:30208
	v_add_f32_e32 v66, v80, v66
	v_add_f32_e32 v66, v81, v66
	v_add_f32_e32 v66, v50, v66
	v_add_f32_e32 v66, v51, v66
	v_cvt_pk_f16_f32 v128, v78, v79
	v_cvt_pk_f16_f32 v129, v80, v81
	ds_read_b64_tr_b16 v[70:71], v186 offset:26624
	ds_read_b64_tr_b16 v[72:73], v186 offset:27136
	v_add_f32_e32 v66, v52, v66
	v_add_f32_e32 v66, v53, v66
	v_add_f32_e32 v66, v54, v66
	v_add_f32_e32 v78, v55, v66
	v_cvt_pk_f16_f32 v118, v50, v51
	v_cvt_pk_f16_f32 v119, v52, v53
	ds_read_b64_tr_b16 v[66:67], v186 offset:30720
	ds_read_b64_tr_b16 v[68:69], v186 offset:31232
	v_add_f32_e32 v50, v56, v78
	v_add_f32_e32 v50, v57, v50
	v_add_f32_e32 v50, v58, v50
	v_add_f32_e32 v50, v59, v50
	v_cvt_pk_f16_f32 v120, v54, v55
	v_cvt_pk_f16_f32 v121, v56, v57
	ds_read_b64_tr_b16 v[54:55], v186 offset:27648
	ds_read_b64_tr_b16 v[56:57], v186 offset:28160
	v_add_f32_e32 v50, v60, v50
	v_add_f32_e32 v50, v61, v50
	v_add_f32_e32 v50, v62, v50
	v_add_f32_e32 v78, v63, v50
	v_cvt_pk_f16_f32 v114, v58, v59
	v_cvt_pk_f16_f32 v115, v60, v61
	ds_read_b64_tr_b16 v[50:51], v186 offset:31744
	ds_read_b64_tr_b16 v[52:53], v186 offset:32256
	v_add_f32_e32 v58, v64, v78
	v_add_f32_e32 v58, v65, v58
	v_add_f32_e32 v58, 0, v58
	v_cvt_pk_f16_f32 v116, v62, v63
	v_cvt_pk_f16_f32 v117, v64, v65
	s_branch .Lsqk_0a
